# v61 + P11 in-loop MoE weight conversion item rewritten as one lean path (SGPR base + 32-bit offsets): ~400 -> ~250 instructions per item
# speedup vs baseline: 1.0091x; 1.0091x over previous
.LBB0_1473:
	s_cmp_gt_i32 s15, 0xbfff
	s_cbranch_scc1 .LBB0_1472
	s_cmpk_gt_i32 s15, 0x7fff
	s_cbranch_scc1 .Lcv11_w2
	s_lshr_b32 s18, s15, 10
	s_mov_b32 s19, 0
	s_lshl_b64 s[2:3], s[18:19], 23
	s_add_u32 s2, s10, s2
	s_addc_u32 s3, s11, s3
	s_lshl_b64 s[18:19], s[18:19], 21
	s_add_u32 s18, s35, s18
	s_addc_u32 s19, s36, s19
	s_and_b32 s6, s15, 0x3c0
	s_lshl_b32 s20, s15, 5
	s_and_b32 s20, s20, 0x7e0
	s_mov_b32 s21, 13
	s_branch .Lcv11_cm
.Lcv11_w2:
	s_add_i32 s18, s15, 0xffff8000
	s_lshl_b32 s6, s18, 1
	s_and_b32 s6, s6, 0x3c0
	s_lshl_b32 s20, s18, 5
	s_and_b32 s20, s20, 0x3e0
	s_lshr_b32 s18, s18, 9
	s_mov_b32 s19, 0
	s_lshl_b64 s[2:3], s[18:19], 22
	s_add_u32 s2, s12, s2
	s_addc_u32 s3, s13, s3
	s_lshl_b64 s[18:19], s[18:19], 20
	s_add_u32 s18, s33, s18
	s_addc_u32 s19, s34, s19
	s_mov_b32 s21, 12
.Lcv11_cm:
	s_lshl_b32 s46, s20, 2
	s_add_u32 s2, s2, s46
	s_addc_u32 s3, s3, 0
	v_and_b32_e32 v4, 31, v158
	v_lshrrev_b32_e32 v5, 5, v158
	v_add_u32_e32 v2, s6, v5
	v_lshlrev_b32_e32 v2, s21, v2
	v_lshl_add_u32 v2, v4, 2, v2
	s_lshl_b32 s46, 2, s21
	v_or_b32_e32 v40, s20, v4
	v_lshlrev_b32_e32 v40, 10, v40
	v_and_b32_e32 v41, 32, v158
	v_add3_u32 v40, v40, v41, s6
	global_load_dword v8, v2, s[2:3]
	v_add_u32_e32 v3, s46, v2
	global_load_dword v9, v3, s[2:3]
	v_add_u32_e32 v2, s46, v3
	global_load_dword v10, v2, s[2:3]
	v_add_u32_e32 v3, s46, v2
	global_load_dword v11, v3, s[2:3]
	v_add_u32_e32 v2, s46, v3
	global_load_dword v12, v2, s[2:3]
	v_add_u32_e32 v3, s46, v2
	global_load_dword v13, v3, s[2:3]
	v_add_u32_e32 v2, s46, v3
	global_load_dword v14, v2, s[2:3]
	v_add_u32_e32 v3, s46, v2
	global_load_dword v15, v3, s[2:3]
	v_add_u32_e32 v2, s46, v3
	global_load_dword v16, v2, s[2:3]
	v_add_u32_e32 v3, s46, v2
	global_load_dword v17, v3, s[2:3]
	v_add_u32_e32 v2, s46, v3
	global_load_dword v18, v2, s[2:3]
	v_add_u32_e32 v3, s46, v2
	global_load_dword v19, v3, s[2:3]
	v_add_u32_e32 v2, s46, v3
	global_load_dword v20, v2, s[2:3]
	v_add_u32_e32 v3, s46, v2
	global_load_dword v21, v3, s[2:3]
	v_add_u32_e32 v2, s46, v3
	global_load_dword v22, v2, s[2:3]
	v_add_u32_e32 v3, s46, v2
	global_load_dword v23, v3, s[2:3]
	v_add_u32_e32 v2, s46, v3
	global_load_dword v24, v2, s[2:3]
	v_add_u32_e32 v3, s46, v2
	global_load_dword v25, v3, s[2:3]
	v_add_u32_e32 v2, s46, v3
	global_load_dword v26, v2, s[2:3]
	v_add_u32_e32 v3, s46, v2
	global_load_dword v27, v3, s[2:3]
	v_add_u32_e32 v2, s46, v3
	global_load_dword v28, v2, s[2:3]
	v_add_u32_e32 v3, s46, v2
	global_load_dword v29, v3, s[2:3]
	v_add_u32_e32 v2, s46, v3
	global_load_dword v30, v2, s[2:3]
	v_add_u32_e32 v3, s46, v2
	global_load_dword v31, v3, s[2:3]
	v_add_u32_e32 v2, s46, v3
	global_load_dword v32, v2, s[2:3]
	v_add_u32_e32 v3, s46, v2
	global_load_dword v33, v3, s[2:3]
	v_add_u32_e32 v2, s46, v3
	global_load_dword v34, v2, s[2:3]
	v_add_u32_e32 v3, s46, v2
	global_load_dword v35, v3, s[2:3]
	v_add_u32_e32 v2, s46, v3
	global_load_dword v36, v2, s[2:3]
	v_add_u32_e32 v3, s46, v2
	global_load_dword v37, v3, s[2:3]
	v_add_u32_e32 v2, s46, v3
	global_load_dword v38, v2, s[2:3]
	v_add_u32_e32 v3, s46, v2
	global_load_dword v39, v3, s[2:3]
	v_lshlrev_b32_e32 v6, 2, v4
	v_add_u32_e32 v6, s23, v6
	v_mul_u32_u24_e32 v41, 0x1080, v5
	v_add_u32_e32 v7, v6, v41
	v_mul_u32_u24_e32 v41, 0x84, v5
	v_add_u32_e32 v6, v6, v41
	s_waitcnt vmcnt(28)
	v_mul_f32_e32 v8, 0x42800000, v8
	v_mul_f32_e32 v9, 0x42800000, v9
	v_mul_f32_e32 v10, 0x42800000, v10
	v_mul_f32_e32 v11, 0x42800000, v11
	ds_write2_b32 v6, v8, v9 offset0:0 offset1:66
	ds_write2_b32 v6, v10, v11 offset0:132 offset1:198
	v_add_u32_e32 v41, 0x400, v6
	s_waitcnt vmcnt(24)
	v_mul_f32_e32 v12, 0x42800000, v12
	v_mul_f32_e32 v13, 0x42800000, v13
	v_mul_f32_e32 v14, 0x42800000, v14
	v_mul_f32_e32 v15, 0x42800000, v15
	ds_write2_b32 v41, v12, v13 offset0:8 offset1:74
	ds_write2_b32 v41, v14, v15 offset0:140 offset1:206
	v_add_u32_e32 v41, 0x800, v6
	s_waitcnt vmcnt(20)
	v_mul_f32_e32 v16, 0x42800000, v16
	v_mul_f32_e32 v17, 0x42800000, v17
	v_mul_f32_e32 v18, 0x42800000, v18
	v_mul_f32_e32 v19, 0x42800000, v19
	ds_write2_b32 v41, v16, v17 offset0:16 offset1:82
	ds_write2_b32 v41, v18, v19 offset0:148 offset1:214
	v_add_u32_e32 v41, 0xc00, v6
	s_waitcnt vmcnt(16)
	v_mul_f32_e32 v20, 0x42800000, v20
	v_mul_f32_e32 v21, 0x42800000, v21
	v_mul_f32_e32 v22, 0x42800000, v22
	v_mul_f32_e32 v23, 0x42800000, v23
	ds_write2_b32 v41, v20, v21 offset0:24 offset1:90
	ds_write2_b32 v41, v22, v23 offset0:156 offset1:222
	v_add_u32_e32 v41, 0x1000, v6
	s_waitcnt vmcnt(12)
	v_mul_f32_e32 v24, 0x42800000, v24
	v_mul_f32_e32 v25, 0x42800000, v25
	v_mul_f32_e32 v26, 0x42800000, v26
	v_mul_f32_e32 v27, 0x42800000, v27
	ds_write2_b32 v41, v24, v25 offset0:32 offset1:98
	ds_write2_b32 v41, v26, v27 offset0:164 offset1:230
	v_add_u32_e32 v41, 0x1400, v6
	s_waitcnt vmcnt(8)
	v_mul_f32_e32 v28, 0x42800000, v28
	v_mul_f32_e32 v29, 0x42800000, v29
	v_mul_f32_e32 v30, 0x42800000, v30
	v_mul_f32_e32 v31, 0x42800000, v31
	ds_write2_b32 v41, v28, v29 offset0:40 offset1:106
	ds_write2_b32 v41, v30, v31 offset0:172 offset1:238
	v_add_u32_e32 v41, 0x1800, v6
	s_waitcnt vmcnt(4)
	v_mul_f32_e32 v32, 0x42800000, v32
	v_mul_f32_e32 v33, 0x42800000, v33
	v_mul_f32_e32 v34, 0x42800000, v34
	v_mul_f32_e32 v35, 0x42800000, v35
	ds_write2_b32 v41, v32, v33 offset0:48 offset1:114
	ds_write2_b32 v41, v34, v35 offset0:180 offset1:246
	v_add_u32_e32 v41, 0x1c00, v6
	s_waitcnt vmcnt(0)
	v_mul_f32_e32 v36, 0x42800000, v36
	v_mul_f32_e32 v37, 0x42800000, v37
	v_mul_f32_e32 v38, 0x42800000, v38
	v_mul_f32_e32 v39, 0x42800000, v39
	ds_write2_b32 v41, v36, v37 offset0:56 offset1:122
	ds_write2_b32 v41, v38, v39 offset0:188 offset1:254
	s_waitcnt lgkmcnt(0)
	ds_read2_b32 v[8:9], v7 offset0:0 offset1:33
	ds_read2_b32 v[10:11], v7 offset0:66 offset1:99
	ds_read2_b32 v[12:13], v7 offset0:132 offset1:165
	ds_read2_b32 v[14:15], v7 offset0:198 offset1:231
	v_add_u32_e32 v41, 0x400, v7
	ds_read2_b32 v[16:17], v41 offset0:8 offset1:41
	ds_read2_b32 v[18:19], v41 offset0:74 offset1:107
	ds_read2_b32 v[20:21], v41 offset0:140 offset1:173
	ds_read2_b32 v[22:23], v41 offset0:206 offset1:239
	v_add_u32_e32 v41, 0x800, v7
	ds_read2_b32 v[24:25], v41 offset0:16 offset1:49
	ds_read2_b32 v[26:27], v41 offset0:82 offset1:115
	ds_read2_b32 v[28:29], v41 offset0:148 offset1:181
	ds_read2_b32 v[30:31], v41 offset0:214 offset1:247
	v_add_u32_e32 v41, 0xc00, v7
	ds_read2_b32 v[32:33], v41 offset0:24 offset1:57
	ds_read2_b32 v[34:35], v41 offset0:90 offset1:123
	ds_read2_b32 v[36:37], v41 offset0:156 offset1:189
	ds_read2_b32 v[38:39], v41 offset0:222 offset1:255
	s_waitcnt lgkmcnt(14)
	v_med3_f32 v8, v8, s39, v162
	v_med3_f32 v9, v9, s39, v162
	v_med3_f32 v10, v10, s39, v162
	v_med3_f32 v11, v11, s39, v162
	v_cvt_pk_fp8_f32 v42, v8, v9
	v_cvt_pk_fp8_f32 v42, v10, v11 op_sel:[0,0,1]
	s_waitcnt lgkmcnt(12)
	v_med3_f32 v12, v12, s39, v162
	v_med3_f32 v13, v13, s39, v162
	v_med3_f32 v14, v14, s39, v162
	v_med3_f32 v15, v15, s39, v162
	v_cvt_pk_fp8_f32 v43, v12, v13
	v_cvt_pk_fp8_f32 v43, v14, v15 op_sel:[0,0,1]
	s_waitcnt lgkmcnt(10)
	v_med3_f32 v16, v16, s39, v162
	v_med3_f32 v17, v17, s39, v162
	v_med3_f32 v18, v18, s39, v162
	v_med3_f32 v19, v19, s39, v162
	v_cvt_pk_fp8_f32 v44, v16, v17
	v_cvt_pk_fp8_f32 v44, v18, v19 op_sel:[0,0,1]
	s_waitcnt lgkmcnt(8)
	v_med3_f32 v20, v20, s39, v162
	v_med3_f32 v21, v21, s39, v162
	v_med3_f32 v22, v22, s39, v162
	v_med3_f32 v23, v23, s39, v162
	v_cvt_pk_fp8_f32 v45, v20, v21
	v_cvt_pk_fp8_f32 v45, v22, v23 op_sel:[0,0,1]
	global_store_dwordx4 v40, v[42:45], s[18:19]
	s_nop 1
	s_waitcnt lgkmcnt(6)
	v_med3_f32 v24, v24, s39, v162
	v_med3_f32 v25, v25, s39, v162
	v_med3_f32 v26, v26, s39, v162
	v_med3_f32 v27, v27, s39, v162
	v_cvt_pk_fp8_f32 v42, v24, v25
	v_cvt_pk_fp8_f32 v42, v26, v27 op_sel:[0,0,1]
	s_waitcnt lgkmcnt(4)
	v_med3_f32 v28, v28, s39, v162
	v_med3_f32 v29, v29, s39, v162
	v_med3_f32 v30, v30, s39, v162
	v_med3_f32 v31, v31, s39, v162
	v_cvt_pk_fp8_f32 v43, v28, v29
	v_cvt_pk_fp8_f32 v43, v30, v31 op_sel:[0,0,1]
	s_waitcnt lgkmcnt(2)
	v_med3_f32 v32, v32, s39, v162
	v_med3_f32 v33, v33, s39, v162
	v_med3_f32 v34, v34, s39, v162
	v_med3_f32 v35, v35, s39, v162
	v_cvt_pk_fp8_f32 v44, v32, v33
	v_cvt_pk_fp8_f32 v44, v34, v35 op_sel:[0,0,1]
	s_waitcnt lgkmcnt(0)
	v_med3_f32 v36, v36, s39, v162
	v_med3_f32 v37, v37, s39, v162
	v_med3_f32 v38, v38, s39, v162
	v_med3_f32 v39, v39, s39, v162
	v_cvt_pk_fp8_f32 v45, v36, v37
	v_cvt_pk_fp8_f32 v45, v38, v39 op_sel:[0,0,1]
	global_store_dwordx4 v40, v[42:45], s[18:19] offset:16
	s_branch .LBB0_1472
